# P8 tile table: tail shared-expert tiles entered as two 128-row tiles (balances the last gate/up round)
# speedup vs baseline: 1.0067x; 1.0067x over previous
; __device__ __forceinline__ void phase7(const Args& a, LAS unsigned char* lds, int tid, int lane, int wave, int vcu, int G) {
;     ...
;             if (blk == 0) {
;                 const int nte = (t + 255) >> 8; int inc2 = nte;
; #pragma unroll
;                 for (int o = 1; o < 64; o <<= 1) { const int v = __shfl_up(inc2, o); if (lane >= o) inc2 += v; }
;                 const int n0 = inc2 - nte; const int ntot = __builtin_amdgcn_readlane(inc2, 63);
;                 for (int j = 0; j < nte; ++j) { tile[n0 + j] = lane; tile[NTILE_MAX + n0 + j] = start + j * 256; tile[2 * NTILE_MAX + n0 + j] = (t - j * 256) < 256 ? (t - j * 256) : 256; }
;                 tile[ntot + lane] = 64; tile[NTILE_MAX + ntot + lane] = SH_ROW0 + lane * 256; tile[2 * NTILE_MAX + ntot + lane] = 256;
;                 if (lane == 0) tile[3 * NTILE_MAX] = ntot + 64;
.LBB0_1166:
	s_or_b64 exec, exec, s[12:13]
	s_add_i32 s38, s33, 0xfffffe00
	s_sub_i32 s34, 64, s38
	s_min_i32 s38, s38, s34
	s_max_i32 s38, s38, 0
	s_sub_i32 s34, 64, s38
	v_subrev_u32_e32 v2, s34, v18
	v_cmp_le_i32_e32 vcc, 0, v2
	v_max_i32_e32 v2, 0, v2
	v_add3_u32 v4, s33, v2, v18
	v_mov_b32_e32 v5, 0
	v_mov_b32_e32 v7, 0
	v_mov_b32_e32 v8, 0x80
	v_cndmask_b32_e32 v9, v60, v8, vcc
	v_lshl_add_u64 v[2:3], v[4:5], 2, s[28:29]
	global_store_dword v[2:3], v59, off
	v_add_u32_e32 v6, 0x2c0, v4
	v_lshl_add_u64 v[2:3], v[6:7], 2, s[28:29]
	global_store_dword v[2:3], v54, off
	v_add_u32_e32 v6, 0x580, v4
	v_lshl_add_u64 v[2:3], v[6:7], 2, s[28:29]
	global_store_dword v[2:3], v9, off
	s_and_saveexec_b64 s[34:35], vcc
	v_add_u32_e32 v4, 1, v4
	v_add_u32_e32 v9, 0x80, v54
	v_lshl_add_u64 v[2:3], v[4:5], 2, s[28:29]
	global_store_dword v[2:3], v59, off
	v_add_u32_e32 v6, 0x2c0, v4
	v_lshl_add_u64 v[2:3], v[6:7], 2, s[28:29]
	global_store_dword v[2:3], v9, off
	v_add_u32_e32 v6, 0x580, v4
	v_lshl_add_u64 v[2:3], v[6:7], 2, s[28:29]
	global_store_dword v[2:3], v8, off
	s_or_b64 exec, exec, s[34:35]
	s_and_saveexec_b64 s[12:13], s[0:1]
	s_cbranch_execz .LBB0_1168
	s_add_i32 s33, s33, 64
	s_add_i32 s33, s33, s38
	v_readlane_b32 s34, v246, 38
	v_mov_b32_e32 v2, s33
	v_readlane_b32 s35, v246, 39
	s_nop 4
	global_store_dword v23, v2, s[34:35]
